# adds RoPE epilogue cos/sin preload (one wait instead of eight load-wait chains per rope tile) to the final stack
# baseline (speedup 1.0000x reference)
; __device__ __forceinline__ unsigned cvt_pk_bf16(float lo, float hi) { unsigned r; asm volatile("v_cvt_pk_bf16_f32 %0, %1, %2" : "=v"(r) : "v"(lo), "v"(hi)); return r; }
;     __device__ __forceinline__ void operator()(AccRef acc, const pg8::Unit& u, int wr, int wc, int fr, int fq) const {
;     ...
;         const int row0 = u.pm * 256 + wr * 64 + fr, col0 = u.pn * 256 + wc * 32 + 8 * fq;
;         const bool rope = u.pn < 8;
; #pragma unroll
;         for (int ai = 0; ai < 2; ++ai)
; #pragma unroll
;             for (int m = 0; m < 4; ++m) {
;                 const int row = row0 + ai * 128 + m * 16, pos = row & (SEQ - 1);
;                 f32x4 cs = {1.f, 1.f, 1.f, 1.f}, sn = {0.f, 0.f, 0.f, 0.f};
;                 if (rope) { cs = *(const f32x4*)(cosT + pos * 64 + 16 * wc + 4 * fq); sn = *(const f32x4*)(sinT + pos * 64 + 16 * wc + 4 * fq); }
;                 bf16_t* rowp = Z + (size_t)row * DIN + col0;
; #pragma unroll
;                 for (int bj = 0; bj < 2; ++bj) {
;                     const f32x4 v0 = acc[ai][bj][m][0] * (1.f / WIN_SCALE), v1 = acc[ai][bj][m][1] * (1.f / WIN_SCALE);
;                     u32x4 w;
;                     w.x = cvt_pk_bf16(v0[0] * cs[0] - v0[1] * sn[0], v0[1] * cs[0] + v0[0] * sn[0]);
;                     w.y = cvt_pk_bf16(v0[2] * cs[1] - v0[3] * sn[1], v0[3] * cs[1] + v0[2] * sn[1]);
;                     w.z = cvt_pk_bf16(v1[0] * cs[2] - v1[1] * sn[2], v1[1] * cs[2] + v1[0] * sn[2]);
;                     w.w = cvt_pk_bf16(v1[2] * cs[3] - v1[3] * sn[3], v1[3] * cs[3] + v1[2] * sn[3]);
;                     *(u32x4*)(rowp + bj * 128) = w;
.LBB0_188:
	v_mov_b32_e32 v0, v181
	v_mov_b32_e32 v34, v180
	s_lshl_b32 s2, s18, 8
	s_nop 15
	s_nop 15
	s_cmp_lt_i32 s55, 8
	v_lshlrev_b32_e32 v2, 2, v34
	s_cselect_b64 s[18:19], -1, 0
	s_add_i32 s2, s2, s41
	v_ashrrev_i32_e32 v3, 31, v2
	s_cmp_gt_i32 s55, 7
	v_add_u32_e32 v42, s2, v0
	v_mov_b32_e32 v1, 0
	v_mov_b32_e32 v0, 1.0
	v_lshlrev_b64 v[32:33], 2, v[2:3]
	v_mov_b32_e32 v2, 1.0
	v_mov_b32_e32 v38, 1.0
	v_mov_b32_e32 v4, 1.0
	v_mov_b32_e32 v36, 1.0
	v_mov_b32_e32 v3, 0
	v_mov_b32_e32 v39, 0
	v_mov_b32_e32 v5, 0
	v_mov_b32_e32 v37, 0
	s_cbranch_scc1 .LBB0_190
	v_lshlrev_b32_e32 v2, 8, v42
	v_and_b32_e32 v192, 0x7ff00, v2
	v_lshl_add_u64 v[2:3], s[14:15], 0, v[192:193]
	v_lshl_add_u64 v[36:37], s[16:17], 0, v[192:193]
	v_lshl_add_u64 v[2:3], v[2:3], 0, v[32:33]
	v_lshl_add_u64 v[36:37], v[36:37], 0, v[32:33]
	v_add_u32_e32 v187, v192, v32
	v_add_u32_e32 v240, 0x1000, v187
	global_load_dwordx4 v[188:191], v240, s[14:15]
	global_load_dwordx4 v[228:231], v240, s[16:17]
	v_add_u32_e32 v215, 0x2000, v187
	global_load_dwordx4 v[194:197], v215, s[14:15]
	global_load_dwordx4 v[232:235], v215, s[16:17]
	v_add_u32_e32 v240, 0x3000, v187
	global_load_dwordx4 v[198:201], v240, s[14:15]
	global_load_dwordx4 v[236:239], v240, s[16:17]
	v_add_u32_e32 v215, 0x8000, v187
	global_load_dwordx4 v[202:205], v215, s[14:15]
	global_load_dwordx4 v[242:245], v215, s[16:17]
	v_add_u32_e32 v240, 0x9000, v187
	global_load_dwordx4 v[216:219], v240, s[14:15]
	global_load_dwordx4 v[246:249], v240, s[16:17]
	v_add_u32_e32 v215, 0xa000, v187
	global_load_dwordx4 v[220:223], v215, s[14:15]
	global_load_dwordx4 v[250:253], v215, s[16:17]
	v_add_u32_e32 v240, 0xb000, v187
	global_load_dwordx4 v[224:227], v240, s[14:15]
	flat_load_dwordx4 v[2:5], v[2:3]
	s_nop 0
	flat_load_dwordx4 v[46:49], v[36:37]
	s_waitcnt vmcnt(0) lgkmcnt(0)
	v_mov_b32_e32 v38, v3
	v_mov_b32_e32 v36, v5
	v_mov_b32_e32 v3, v46
	v_mov_b32_e32 v39, v47
	v_mov_b32_e32 v5, v48
	v_mov_b32_e32 v37, v49
.LBB0_190:
	s_lshl_b32 s2, s55, 8
	s_or_b32 s2, s2, s42
	v_lshl_add_u32 v34, v34, 3, s2
	v_mov_b64_e32 v[46:47], s[8:9]
	v_ashrrev_i32_e32 v35, 31, v34
	v_mad_i64_i32 v[46:47], s[2:3], v42, s85, v[46:47]
	v_lshl_add_u64 v[50:51], v[34:35], 1, v[46:47]
	v_pk_mul_f32 v[46:47], v[170:171], v[2:3]
	v_mov_b32_e32 v56, v3
	v_mov_b32_e32 v57, v2
	v_sub_f32_e32 v43, v46, v47
	v_pk_mul_f32 v[46:47], v[170:171], v[56:57]
	v_pk_mul_f32 v[48:49], v[160:161], v[38:39]
	v_add_f32_e32 v46, v47, v46
	v_mov_b32_e32 v58, v39
	v_mov_b32_e32 v59, v38
	v_cvt_pk_bf16_f32 v46, v43, v46
	v_sub_f32_e32 v43, v48, v49
	v_pk_mul_f32 v[48:49], v[160:161], v[58:59]
	v_mov_b32_e32 v64, v5
	v_add_f32_e32 v47, v49, v48
	v_pk_mul_f32 v[48:49], v[164:165], v[4:5]
	v_mov_b32_e32 v65, v4
	v_cvt_pk_bf16_f32 v47, v43, v47
	v_sub_f32_e32 v43, v48, v49
	v_pk_mul_f32 v[48:49], v[164:165], v[64:65]
	v_pk_mul_f32 v[66:67], v[156:157], v[36:37]
	v_add_f32_e32 v48, v49, v48
	v_cvt_pk_bf16_f32 v48, v43, v48
	v_sub_f32_e32 v43, v66, v67
	v_mov_b32_e32 v66, v37
	v_mov_b32_e32 v67, v36
	v_pk_mul_f32 v[72:73], v[156:157], v[66:67]
	v_pk_mul_f32 v[2:3], v[168:169], v[2:3]
	v_add_f32_e32 v49, v73, v72
	v_cvt_pk_bf16_f32 v49, v43, v49
	v_sub_f32_e32 v43, v2, v3
	v_pk_mul_f32 v[2:3], v[168:169], v[56:57]
	v_pk_mul_f32 v[38:39], v[162:163], v[38:39]
	v_add_f32_e32 v2, v3, v2
	v_sub_f32_e32 v3, v38, v39
	v_pk_mul_f32 v[38:39], v[162:163], v[58:59]
	v_pk_mul_f32 v[4:5], v[166:167], v[4:5]
	v_add_f32_e32 v38, v39, v38
	flat_store_dwordx4 v[50:51], v[46:49]
	v_cvt_pk_bf16_f32 v2, v43, v2
	v_cvt_pk_bf16_f32 v3, v3, v38
	v_sub_f32_e32 v38, v4, v5
	v_pk_mul_f32 v[4:5], v[166:167], v[64:65]
	v_pk_mul_f32 v[36:37], v[158:159], v[36:37]
	v_add_f32_e32 v4, v5, v4
	v_sub_f32_e32 v5, v36, v37
	v_pk_mul_f32 v[36:37], v[158:159], v[66:67]
	v_cvt_pk_bf16_f32 v4, v38, v4
	v_add_u32_e32 v38, 16, v42
	v_add_f32_e32 v36, v37, v36
	v_cvt_pk_bf16_f32 v5, v5, v36
	flat_store_dwordx4 v[50:51], v[2:5] offset:256
	s_andn2_b64 vcc, exec, s[18:19]
	v_mov_b32_e32 v36, 1.0
	v_cndmask_b32_e64 v2, 0, 1, s[18:19]
	v_cmp_ne_u32_e64 s[2:3], 1, v2
	v_mov_b32_e32 v2, 1.0
	v_mov_b32_e32 v4, 1.0
	v_mov_b32_e32 v37, 0
	v_mov_b32_e32 v3, 0
	v_mov_b32_e32 v5, 0
	s_cbranch_vccnz .LBB0_192
	v_mov_b32_e32 v0, v188
	v_mov_b32_e32 v1, v189
	v_mov_b32_e32 v2, v190
	v_mov_b32_e32 v3, v191
	v_mov_b32_e32 v46, v228
	v_mov_b32_e32 v47, v229
	v_mov_b32_e32 v48, v230
	v_mov_b32_e32 v49, v231
	v_mov_b32_e32 v36, v1
	v_mov_b32_e32 v4, v3
	v_mov_b32_e32 v1, v46
	v_mov_b32_e32 v37, v47
	v_mov_b32_e32 v3, v48
	v_mov_b32_e32 v5, v49
; __device__ __forceinline__ unsigned cvt_pk_bf16(float lo, float hi) { unsigned r; asm volatile("v_cvt_pk_bf16_f32 %0, %1, %2" : "=v"(r) : "v"(lo), "v"(hi)); return r; }
;     __device__ __forceinline__ void operator()(AccRef acc, const pg8::Unit& u, int wr, int wc, int fr, int fq) const {
;     ...
;             for (int m = 0; m < 4; ++m) {
;                 const int row = row0 + ai * 128 + m * 16, pos = row & (SEQ - 1);
;                 f32x4 cs = {1.f, 1.f, 1.f, 1.f}, sn = {0.f, 0.f, 0.f, 0.f};
;                 if (rope) { cs = *(const f32x4*)(cosT + pos * 64 + 16 * wc + 4 * fq); sn = *(const f32x4*)(sinT + pos * 64 + 16 * wc + 4 * fq); }
;                 bf16_t* rowp = Z + (size_t)row * DIN + col0;
; #pragma unroll
;                 for (int bj = 0; bj < 2; ++bj) {
;                     const f32x4 v0 = acc[ai][bj][m][0] * (1.f / WIN_SCALE), v1 = acc[ai][bj][m][1] * (1.f / WIN_SCALE);
;                     u32x4 w;
;                     w.x = cvt_pk_bf16(v0[0] * cs[0] - v0[1] * sn[0], v0[1] * cs[0] + v0[0] * sn[0]);
;                     w.y = cvt_pk_bf16(v0[2] * cs[1] - v0[3] * sn[1], v0[3] * cs[1] + v0[2] * sn[1]);
;                     w.z = cvt_pk_bf16(v1[0] * cs[2] - v1[1] * sn[2], v1[1] * cs[2] + v1[0] * sn[2]);
;                     w.w = cvt_pk_bf16(v1[2] * cs[3] - v1[3] * sn[3], v1[3] * cs[3] + v1[2] * sn[3]);
;                     *(u32x4*)(rowp + bj * 128) = w;
.LBB0_192:
	v_mov_b64_e32 v[46:47], s[8:9]
	v_mad_i64_i32 v[38:39], s[18:19], v38, s85, v[46:47]
	v_pk_mul_f32 v[46:47], v[154:155], v[0:1]
	v_mov_b32_e32 v50, v1
	v_mov_b32_e32 v51, v0
	v_sub_f32_e32 v43, v46, v47
	v_pk_mul_f32 v[46:47], v[154:155], v[50:51]
	v_pk_mul_f32 v[48:49], v[150:151], v[36:37]
	v_add_f32_e32 v46, v47, v46
	v_mov_b32_e32 v56, v37
	v_mov_b32_e32 v57, v36
	v_cvt_pk_bf16_f32 v46, v43, v46
	v_sub_f32_e32 v43, v48, v49
	v_pk_mul_f32 v[48:49], v[150:151], v[56:57]
	v_mov_b32_e32 v58, v3
	v_add_f32_e32 v47, v49, v48
	v_pk_mul_f32 v[48:49], v[146:147], v[2:3]
	v_mov_b32_e32 v59, v2
	v_cvt_pk_bf16_f32 v47, v43, v47
	v_sub_f32_e32 v43, v48, v49
	v_pk_mul_f32 v[48:49], v[146:147], v[58:59]
	v_pk_mul_f32 v[64:65], v[140:141], v[4:5]
	v_add_f32_e32 v48, v49, v48
	v_cvt_pk_bf16_f32 v48, v43, v48
	v_sub_f32_e32 v43, v64, v65
	v_mov_b32_e32 v64, v5
	v_mov_b32_e32 v65, v4
	v_pk_mul_f32 v[66:67], v[140:141], v[64:65]
	v_pk_mul_f32 v[0:1], v[152:153], v[0:1]
	v_add_f32_e32 v49, v67, v66
	v_cvt_pk_bf16_f32 v49, v43, v49
	v_sub_f32_e32 v43, v0, v1
	v_pk_mul_f32 v[0:1], v[152:153], v[50:51]
	v_pk_mul_f32 v[36:37], v[144:145], v[36:37]
	v_add_f32_e32 v0, v1, v0
	v_sub_f32_e32 v1, v36, v37
	v_pk_mul_f32 v[36:37], v[144:145], v[56:57]
	v_lshl_add_u64 v[38:39], v[34:35], 1, v[38:39]
	v_add_f32_e32 v36, v37, v36
	v_pk_mul_f32 v[2:3], v[148:149], v[2:3]
	flat_store_dwordx4 v[38:39], v[46:49]
	v_cvt_pk_bf16_f32 v0, v43, v0
	v_cvt_pk_bf16_f32 v1, v1, v36
	v_sub_f32_e32 v36, v2, v3
	v_pk_mul_f32 v[2:3], v[148:149], v[58:59]
	v_pk_mul_f32 v[4:5], v[142:143], v[4:5]
	v_add_f32_e32 v2, v3, v2
	v_sub_f32_e32 v3, v4, v5
	v_pk_mul_f32 v[4:5], v[142:143], v[64:65]
	v_cvt_pk_bf16_f32 v2, v36, v2
	v_add_u32_e32 v43, 32, v42
	v_add_f32_e32 v4, v5, v4
	v_cvt_pk_bf16_f32 v3, v3, v4
	flat_store_dwordx4 v[38:39], v[0:3] offset:256
	s_and_b64 vcc, exec, s[2:3]
	v_mov_b32_e32 v38, 1.0
	v_mov_b32_e32 v1, 0
	v_mov_b32_e32 v0, 1.0
	v_mov_b32_e32 v2, 1.0
	v_mov_b32_e32 v4, 1.0
	v_mov_b32_e32 v36, 1.0
	v_mov_b32_e32 v3, 0
	v_mov_b32_e32 v39, 0
	v_mov_b32_e32 v5, 0
	v_mov_b32_e32 v37, 0
	s_cbranch_vccnz .LBB0_194
	v_mov_b32_e32 v2, v194
	v_mov_b32_e32 v3, v195
	v_mov_b32_e32 v4, v196
	v_mov_b32_e32 v5, v197
	v_mov_b32_e32 v46, v232
	v_mov_b32_e32 v47, v233
	v_mov_b32_e32 v48, v234
	v_mov_b32_e32 v49, v235
	v_mov_b32_e32 v38, v3
	v_mov_b32_e32 v36, v5
	v_mov_b32_e32 v3, v46
	v_mov_b32_e32 v39, v47
	v_mov_b32_e32 v5, v48
	v_mov_b32_e32 v37, v49
.LBB0_194:
	v_mov_b64_e32 v[46:47], s[8:9]
	v_mad_i64_i32 v[46:47], s[18:19], v43, s85, v[46:47]
	v_lshl_add_u64 v[50:51], v[34:35], 1, v[46:47]
	v_pk_mul_f32 v[46:47], v[138:139], v[2:3]
	v_mov_b32_e32 v56, v3
	v_mov_b32_e32 v57, v2
	v_sub_f32_e32 v43, v46, v47
	v_pk_mul_f32 v[46:47], v[138:139], v[56:57]
	v_pk_mul_f32 v[48:49], v[132:133], v[38:39]
	v_add_f32_e32 v46, v47, v46
	v_mov_b32_e32 v58, v39
	v_mov_b32_e32 v59, v38
	v_cvt_pk_bf16_f32 v46, v43, v46
	v_sub_f32_e32 v43, v48, v49
	v_pk_mul_f32 v[48:49], v[132:133], v[58:59]
	v_mov_b32_e32 v64, v5
	v_add_f32_e32 v47, v49, v48
	v_pk_mul_f32 v[48:49], v[130:131], v[4:5]
	v_mov_b32_e32 v65, v4
	v_cvt_pk_bf16_f32 v47, v43, v47
	v_sub_f32_e32 v43, v48, v49
	v_pk_mul_f32 v[48:49], v[130:131], v[64:65]
	v_pk_mul_f32 v[66:67], v[124:125], v[36:37]
	v_add_f32_e32 v48, v49, v48
	v_cvt_pk_bf16_f32 v48, v43, v48
	v_sub_f32_e32 v43, v66, v67
	v_mov_b32_e32 v66, v37
	v_mov_b32_e32 v67, v36
	v_pk_mul_f32 v[72:73], v[124:125], v[66:67]
	v_pk_mul_f32 v[2:3], v[136:137], v[2:3]
	v_add_f32_e32 v49, v73, v72
	v_cvt_pk_bf16_f32 v49, v43, v49
	v_sub_f32_e32 v43, v2, v3
	v_pk_mul_f32 v[2:3], v[136:137], v[56:57]
	v_pk_mul_f32 v[38:39], v[128:129], v[38:39]
	v_add_f32_e32 v2, v3, v2
	v_sub_f32_e32 v3, v38, v39
	v_pk_mul_f32 v[38:39], v[128:129], v[58:59]
	v_pk_mul_f32 v[4:5], v[134:135], v[4:5]
	v_add_f32_e32 v38, v39, v38
	flat_store_dwordx4 v[50:51], v[46:49]
	v_cvt_pk_bf16_f32 v2, v43, v2
	v_cvt_pk_bf16_f32 v3, v3, v38
	v_sub_f32_e32 v38, v4, v5
	v_pk_mul_f32 v[4:5], v[134:135], v[64:65]
	v_pk_mul_f32 v[36:37], v[126:127], v[36:37]
	v_add_f32_e32 v4, v5, v4
	v_sub_f32_e32 v5, v36, v37
	v_pk_mul_f32 v[36:37], v[126:127], v[66:67]
	v_cvt_pk_bf16_f32 v4, v38, v4
	v_add_u32_e32 v38, 48, v42
	v_add_f32_e32 v36, v37, v36
	v_cvt_pk_bf16_f32 v5, v5, v36
	flat_store_dwordx4 v[50:51], v[2:5] offset:256
	s_and_b64 vcc, exec, s[2:3]
	v_mov_b32_e32 v36, 1.0
	v_mov_b32_e32 v2, 1.0
	v_mov_b32_e32 v4, 1.0
	v_mov_b32_e32 v37, 0
	v_mov_b32_e32 v3, 0
	v_mov_b32_e32 v5, 0
	s_cbranch_vccnz .LBB0_196
	v_mov_b32_e32 v0, v198
	v_mov_b32_e32 v1, v199
	v_mov_b32_e32 v2, v200
	v_mov_b32_e32 v3, v201
	v_mov_b32_e32 v46, v236
	v_mov_b32_e32 v47, v237
	v_mov_b32_e32 v48, v238
	v_mov_b32_e32 v49, v239
	v_mov_b32_e32 v36, v1
	v_mov_b32_e32 v4, v3
	v_mov_b32_e32 v1, v46
	v_mov_b32_e32 v37, v47
	v_mov_b32_e32 v3, v48
	v_mov_b32_e32 v5, v49
; __device__ __forceinline__ unsigned cvt_pk_bf16(float lo, float hi) { unsigned r; asm volatile("v_cvt_pk_bf16_f32 %0, %1, %2" : "=v"(r) : "v"(lo), "v"(hi)); return r; }
;     __device__ __forceinline__ void operator()(AccRef acc, const pg8::Unit& u, int wr, int wc, int fr, int fq) const {
;     ...
;             for (int m = 0; m < 4; ++m) {
;                 const int row = row0 + ai * 128 + m * 16, pos = row & (SEQ - 1);
;                 f32x4 cs = {1.f, 1.f, 1.f, 1.f}, sn = {0.f, 0.f, 0.f, 0.f};
;                 if (rope) { cs = *(const f32x4*)(cosT + pos * 64 + 16 * wc + 4 * fq); sn = *(const f32x4*)(sinT + pos * 64 + 16 * wc + 4 * fq); }
;                 bf16_t* rowp = Z + (size_t)row * DIN + col0;
; #pragma unroll
;                 for (int bj = 0; bj < 2; ++bj) {
;                     const f32x4 v0 = acc[ai][bj][m][0] * (1.f / WIN_SCALE), v1 = acc[ai][bj][m][1] * (1.f / WIN_SCALE);
;                     u32x4 w;
;                     w.x = cvt_pk_bf16(v0[0] * cs[0] - v0[1] * sn[0], v0[1] * cs[0] + v0[0] * sn[0]);
;                     w.y = cvt_pk_bf16(v0[2] * cs[1] - v0[3] * sn[1], v0[3] * cs[1] + v0[2] * sn[1]);
;                     w.z = cvt_pk_bf16(v1[0] * cs[2] - v1[1] * sn[2], v1[1] * cs[2] + v1[0] * sn[2]);
;                     w.w = cvt_pk_bf16(v1[2] * cs[3] - v1[3] * sn[3], v1[3] * cs[3] + v1[2] * sn[3]);
;                     *(u32x4*)(rowp + bj * 128) = w;
.LBB0_196:
	v_mov_b64_e32 v[46:47], s[8:9]
	v_mad_i64_i32 v[38:39], s[18:19], v38, s85, v[46:47]
	v_pk_mul_f32 v[46:47], v[118:119], v[0:1]
	v_mov_b32_e32 v50, v1
	v_mov_b32_e32 v51, v0
	v_sub_f32_e32 v43, v46, v47
	v_pk_mul_f32 v[46:47], v[118:119], v[50:51]
	v_pk_mul_f32 v[48:49], v[116:117], v[36:37]
	v_add_f32_e32 v46, v47, v46
	v_mov_b32_e32 v56, v37
	v_mov_b32_e32 v57, v36
	v_cvt_pk_bf16_f32 v46, v43, v46
	v_sub_f32_e32 v43, v48, v49
	v_pk_mul_f32 v[48:49], v[116:117], v[56:57]
	v_mov_b32_e32 v58, v3
	v_add_f32_e32 v47, v49, v48
	v_pk_mul_f32 v[48:49], v[110:111], v[2:3]
	v_mov_b32_e32 v59, v2
	v_cvt_pk_bf16_f32 v47, v43, v47
	v_sub_f32_e32 v43, v48, v49
	v_pk_mul_f32 v[48:49], v[110:111], v[58:59]
	v_pk_mul_f32 v[64:65], v[104:105], v[4:5]
	v_add_f32_e32 v48, v49, v48
	v_cvt_pk_bf16_f32 v48, v43, v48
	v_sub_f32_e32 v43, v64, v65
	v_mov_b32_e32 v64, v5
	v_mov_b32_e32 v65, v4
	v_pk_mul_f32 v[66:67], v[104:105], v[64:65]
	v_pk_mul_f32 v[0:1], v[114:115], v[0:1]
	v_add_f32_e32 v49, v67, v66
	v_cvt_pk_bf16_f32 v49, v43, v49
	v_sub_f32_e32 v43, v0, v1
	v_pk_mul_f32 v[0:1], v[114:115], v[50:51]
	v_pk_mul_f32 v[36:37], v[108:109], v[36:37]
	v_add_f32_e32 v0, v1, v0
	v_sub_f32_e32 v1, v36, v37
	v_pk_mul_f32 v[36:37], v[108:109], v[56:57]
	v_lshl_add_u64 v[38:39], v[34:35], 1, v[38:39]
	v_add_f32_e32 v36, v37, v36
	v_pk_mul_f32 v[2:3], v[112:113], v[2:3]
	flat_store_dwordx4 v[38:39], v[46:49]
	v_cvt_pk_bf16_f32 v0, v43, v0
	v_cvt_pk_bf16_f32 v1, v1, v36
	v_sub_f32_e32 v36, v2, v3
	v_pk_mul_f32 v[2:3], v[112:113], v[58:59]
	v_pk_mul_f32 v[4:5], v[106:107], v[4:5]
	v_add_f32_e32 v2, v3, v2
	v_sub_f32_e32 v3, v4, v5
	v_pk_mul_f32 v[4:5], v[106:107], v[64:65]
	v_cvt_pk_bf16_f32 v2, v36, v2
	v_add_u32_e32 v43, 0x80, v42
	v_add_f32_e32 v4, v5, v4
	v_cvt_pk_bf16_f32 v3, v3, v4
	flat_store_dwordx4 v[38:39], v[0:3] offset:256
	s_and_b64 vcc, exec, s[2:3]
	v_mov_b32_e32 v38, 1.0
	v_mov_b32_e32 v1, 0
	v_mov_b32_e32 v0, 1.0
	v_mov_b32_e32 v2, 1.0
	v_mov_b32_e32 v4, 1.0
	v_mov_b32_e32 v36, 1.0
	v_mov_b32_e32 v3, 0
	v_mov_b32_e32 v39, 0
	v_mov_b32_e32 v5, 0
	v_mov_b32_e32 v37, 0
	s_cbranch_vccnz .LBB0_198
	v_mov_b32_e32 v2, v202
	v_mov_b32_e32 v3, v203
	v_mov_b32_e32 v4, v204
	v_mov_b32_e32 v5, v205
	v_mov_b32_e32 v46, v242
	v_mov_b32_e32 v47, v243
	v_mov_b32_e32 v48, v244
	v_mov_b32_e32 v49, v245
	v_mov_b32_e32 v38, v3
	v_mov_b32_e32 v36, v5
	v_mov_b32_e32 v3, v46
	v_mov_b32_e32 v39, v47
	v_mov_b32_e32 v5, v48
	v_mov_b32_e32 v37, v49
.LBB0_198:
	v_mov_b64_e32 v[46:47], s[8:9]
	v_mad_i64_i32 v[46:47], s[18:19], v43, s85, v[46:47]
	v_lshl_add_u64 v[50:51], v[34:35], 1, v[46:47]
	v_pk_mul_f32 v[46:47], v[102:103], v[2:3]
	v_mov_b32_e32 v56, v3
	v_mov_b32_e32 v57, v2
	v_sub_f32_e32 v43, v46, v47
	v_pk_mul_f32 v[46:47], v[102:103], v[56:57]
	v_pk_mul_f32 v[48:49], v[96:97], v[38:39]
	v_add_f32_e32 v46, v47, v46
	v_mov_b32_e32 v58, v39
	v_mov_b32_e32 v59, v38
	v_cvt_pk_bf16_f32 v46, v43, v46
	v_sub_f32_e32 v43, v48, v49
	v_pk_mul_f32 v[48:49], v[96:97], v[58:59]
	v_mov_b32_e32 v64, v5
	v_add_f32_e32 v47, v49, v48
	v_pk_mul_f32 v[48:49], v[94:95], v[4:5]
	v_mov_b32_e32 v65, v4
	v_cvt_pk_bf16_f32 v47, v43, v47
	v_sub_f32_e32 v43, v48, v49
	v_pk_mul_f32 v[48:49], v[94:95], v[64:65]
	v_pk_mul_f32 v[66:67], v[90:91], v[36:37]
	v_add_f32_e32 v48, v49, v48
	v_cvt_pk_bf16_f32 v48, v43, v48
	v_sub_f32_e32 v43, v66, v67
	v_mov_b32_e32 v66, v37
	v_mov_b32_e32 v67, v36
	v_pk_mul_f32 v[72:73], v[90:91], v[66:67]
	v_pk_mul_f32 v[2:3], v[100:101], v[2:3]
	v_add_f32_e32 v49, v73, v72
	v_cvt_pk_bf16_f32 v49, v43, v49
	v_sub_f32_e32 v43, v2, v3
	v_pk_mul_f32 v[2:3], v[100:101], v[56:57]
	v_pk_mul_f32 v[38:39], v[92:93], v[38:39]
	v_add_f32_e32 v2, v3, v2
	v_sub_f32_e32 v3, v38, v39
	v_pk_mul_f32 v[38:39], v[92:93], v[58:59]
	v_pk_mul_f32 v[4:5], v[98:99], v[4:5]
	v_add_f32_e32 v38, v39, v38
	flat_store_dwordx4 v[50:51], v[46:49]
	v_cvt_pk_bf16_f32 v2, v43, v2
	v_cvt_pk_bf16_f32 v3, v3, v38
	v_sub_f32_e32 v38, v4, v5
	v_pk_mul_f32 v[4:5], v[98:99], v[64:65]
	v_pk_mul_f32 v[36:37], v[88:89], v[36:37]
	v_add_f32_e32 v4, v5, v4
	v_sub_f32_e32 v5, v36, v37
	v_pk_mul_f32 v[36:37], v[88:89], v[66:67]
	v_cvt_pk_bf16_f32 v4, v38, v4
	v_add_u32_e32 v38, 0x90, v42
	v_add_f32_e32 v36, v37, v36
	v_cvt_pk_bf16_f32 v5, v5, v36
	flat_store_dwordx4 v[50:51], v[2:5] offset:256
	s_and_b64 vcc, exec, s[2:3]
	v_mov_b32_e32 v36, 1.0
	v_mov_b32_e32 v2, 1.0
	v_mov_b32_e32 v4, 1.0
	v_mov_b32_e32 v37, 0
	v_mov_b32_e32 v3, 0
	v_mov_b32_e32 v5, 0
	s_cbranch_vccnz .LBB0_200
	v_mov_b32_e32 v0, v216
	v_mov_b32_e32 v1, v217
	v_mov_b32_e32 v2, v218
	v_mov_b32_e32 v3, v219
	v_mov_b32_e32 v46, v246
	v_mov_b32_e32 v47, v247
	v_mov_b32_e32 v48, v248
	v_mov_b32_e32 v49, v249
	v_mov_b32_e32 v36, v1
	v_mov_b32_e32 v4, v3
	v_mov_b32_e32 v1, v46
	v_mov_b32_e32 v37, v47
	v_mov_b32_e32 v3, v48
	v_mov_b32_e32 v5, v49
; __device__ __forceinline__ unsigned cvt_pk_bf16(float lo, float hi) { unsigned r; asm volatile("v_cvt_pk_bf16_f32 %0, %1, %2" : "=v"(r) : "v"(lo), "v"(hi)); return r; }
;     __device__ __forceinline__ void operator()(AccRef acc, const pg8::Unit& u, int wr, int wc, int fr, int fq) const {
;     ...
;                 const int row = row0 + ai * 128 + m * 16, pos = row & (SEQ - 1);
;                 f32x4 cs = {1.f, 1.f, 1.f, 1.f}, sn = {0.f, 0.f, 0.f, 0.f};
;                 if (rope) { cs = *(const f32x4*)(cosT + pos * 64 + 16 * wc + 4 * fq); sn = *(const f32x4*)(sinT + pos * 64 + 16 * wc + 4 * fq); }
;                 bf16_t* rowp = Z + (size_t)row * DIN + col0;
; #pragma unroll
;                 for (int bj = 0; bj < 2; ++bj) {
;                     const f32x4 v0 = acc[ai][bj][m][0] * (1.f / WIN_SCALE), v1 = acc[ai][bj][m][1] * (1.f / WIN_SCALE);
;                     u32x4 w;
;                     w.x = cvt_pk_bf16(v0[0] * cs[0] - v0[1] * sn[0], v0[1] * cs[0] + v0[0] * sn[0]);
;                     w.y = cvt_pk_bf16(v0[2] * cs[1] - v0[3] * sn[1], v0[3] * cs[1] + v0[2] * sn[1]);
;                     w.z = cvt_pk_bf16(v1[0] * cs[2] - v1[1] * sn[2], v1[1] * cs[2] + v1[0] * sn[2]);
;                     w.w = cvt_pk_bf16(v1[2] * cs[3] - v1[3] * sn[3], v1[3] * cs[3] + v1[2] * sn[3]);
;                     *(u32x4*)(rowp + bj * 128) = w;
.LBB0_200:
	v_mov_b64_e32 v[46:47], s[8:9]
	v_mad_i64_i32 v[38:39], s[18:19], v38, s85, v[46:47]
	v_pk_mul_f32 v[46:47], v[84:85], v[0:1]
	v_mov_b32_e32 v50, v1
	v_mov_b32_e32 v51, v0
	v_sub_f32_e32 v43, v46, v47
	v_pk_mul_f32 v[46:47], v[84:85], v[50:51]
	v_pk_mul_f32 v[48:49], v[76:77], v[36:37]
	v_add_f32_e32 v46, v47, v46
	v_mov_b32_e32 v56, v37
	v_mov_b32_e32 v57, v36
	v_cvt_pk_bf16_f32 v46, v43, v46
	v_sub_f32_e32 v43, v48, v49
	v_pk_mul_f32 v[48:49], v[76:77], v[56:57]
	v_mov_b32_e32 v58, v3
	v_add_f32_e32 v47, v49, v48
	v_pk_mul_f32 v[48:49], v[70:71], v[2:3]
	v_mov_b32_e32 v59, v2
	v_cvt_pk_bf16_f32 v47, v43, v47
	v_sub_f32_e32 v43, v48, v49
	v_pk_mul_f32 v[48:49], v[70:71], v[58:59]
	v_pk_mul_f32 v[64:65], v[68:69], v[4:5]
	v_add_f32_e32 v48, v49, v48
	v_cvt_pk_bf16_f32 v48, v43, v48
	v_sub_f32_e32 v43, v64, v65
	v_mov_b32_e32 v64, v5
	v_mov_b32_e32 v65, v4
	v_pk_mul_f32 v[66:67], v[68:69], v[64:65]
	v_pk_mul_f32 v[0:1], v[78:79], v[0:1]
	v_add_f32_e32 v49, v67, v66
	v_cvt_pk_bf16_f32 v49, v43, v49
	v_sub_f32_e32 v43, v0, v1
	v_pk_mul_f32 v[0:1], v[78:79], v[50:51]
	v_pk_mul_f32 v[36:37], v[62:63], v[36:37]
	v_add_f32_e32 v0, v1, v0
	v_sub_f32_e32 v1, v36, v37
	v_pk_mul_f32 v[36:37], v[62:63], v[56:57]
	v_lshl_add_u64 v[38:39], v[34:35], 1, v[38:39]
	v_add_f32_e32 v36, v37, v36
	v_pk_mul_f32 v[2:3], v[60:61], v[2:3]
	flat_store_dwordx4 v[38:39], v[46:49]
	v_cvt_pk_bf16_f32 v0, v43, v0
	v_cvt_pk_bf16_f32 v1, v1, v36
	v_sub_f32_e32 v36, v2, v3
	v_pk_mul_f32 v[2:3], v[60:61], v[58:59]
	v_pk_mul_f32 v[4:5], v[54:55], v[4:5]
	v_add_f32_e32 v2, v3, v2
	v_sub_f32_e32 v3, v4, v5
	v_pk_mul_f32 v[4:5], v[54:55], v[64:65]
	v_cvt_pk_bf16_f32 v2, v36, v2
	v_add_u32_e32 v43, 0xa0, v42
	v_add_f32_e32 v4, v5, v4
	v_cvt_pk_bf16_f32 v3, v3, v4
	flat_store_dwordx4 v[38:39], v[0:3] offset:256
	s_and_b64 vcc, exec, s[2:3]
	v_mov_b32_e32 v38, 1.0
	v_mov_b32_e32 v1, 0
	v_mov_b32_e32 v0, 1.0
	v_mov_b32_e32 v2, 1.0
	v_mov_b32_e32 v4, 1.0
	v_mov_b32_e32 v36, 1.0
	v_mov_b32_e32 v3, 0
	v_mov_b32_e32 v39, 0
	v_mov_b32_e32 v5, 0
	v_mov_b32_e32 v37, 0
	s_cbranch_vccnz .LBB0_202
	v_mov_b32_e32 v2, v220
	v_mov_b32_e32 v3, v221
	v_mov_b32_e32 v4, v222
	v_mov_b32_e32 v5, v223
	v_mov_b32_e32 v46, v250
	v_mov_b32_e32 v47, v251
	v_mov_b32_e32 v48, v252
	v_mov_b32_e32 v49, v253
	v_mov_b32_e32 v38, v3
	v_mov_b32_e32 v36, v5
	v_mov_b32_e32 v3, v46
	v_mov_b32_e32 v39, v47
	v_mov_b32_e32 v5, v48
	v_mov_b32_e32 v37, v49
.LBB0_202:
	v_mov_b64_e32 v[46:47], s[8:9]
	v_mad_i64_i32 v[46:47], s[18:19], v43, s85, v[46:47]
	v_lshl_add_u64 v[50:51], v[34:35], 1, v[46:47]
	v_pk_mul_f32 v[46:47], v[52:53], v[2:3]
	v_mov_b32_e32 v54, v3
	v_mov_b32_e32 v55, v2
	v_sub_f32_e32 v43, v46, v47
	v_pk_mul_f32 v[46:47], v[52:53], v[54:55]
	v_mov_b32_e32 v52, v39
	v_mov_b32_e32 v53, v38
	v_pk_mul_f32 v[48:49], v[30:31], v[38:39]
	v_pk_mul_f32 v[30:31], v[30:31], v[52:53]
	v_add_f32_e32 v46, v47, v46
	v_add_f32_e32 v30, v31, v30
	v_cvt_pk_bf16_f32 v46, v43, v46
	v_sub_f32_e32 v43, v48, v49
	v_cvt_pk_bf16_f32 v47, v43, v30
	v_pk_mul_f32 v[30:31], v[28:29], v[4:5]
	v_pk_mul_f32 v[2:3], v[44:45], v[2:3]
	v_sub_f32_e32 v43, v30, v31
	v_mov_b32_e32 v30, v5
	v_mov_b32_e32 v31, v4
	v_pk_mul_f32 v[28:29], v[28:29], v[30:31]
	v_pk_mul_f32 v[4:5], v[40:41], v[4:5]
	v_add_f32_e32 v28, v29, v28
	v_cvt_pk_bf16_f32 v48, v43, v28
	v_pk_mul_f32 v[28:29], v[22:23], v[36:37]
	s_and_b64 vcc, exec, s[2:3]
	v_sub_f32_e32 v43, v28, v29
	v_mov_b32_e32 v28, v37
	v_mov_b32_e32 v29, v36
	v_pk_mul_f32 v[22:23], v[22:23], v[28:29]
	s_nop 0
	v_add_f32_e32 v22, v23, v22
	v_cvt_pk_bf16_f32 v49, v43, v22
	v_sub_f32_e32 v22, v2, v3
	v_pk_mul_f32 v[2:3], v[44:45], v[54:55]
	flat_store_dwordx4 v[50:51], v[46:49]
	v_add_f32_e32 v2, v3, v2
	v_cvt_pk_bf16_f32 v2, v22, v2
	v_pk_mul_f32 v[22:23], v[26:27], v[38:39]
	s_nop 0
	v_sub_f32_e32 v3, v22, v23
	v_pk_mul_f32 v[22:23], v[26:27], v[52:53]
	s_nop 0
	v_add_f32_e32 v22, v23, v22
	v_cvt_pk_bf16_f32 v3, v3, v22
	v_sub_f32_e32 v22, v4, v5
	v_pk_mul_f32 v[4:5], v[40:41], v[30:31]
	s_nop 0
	v_add_f32_e32 v4, v5, v4
	v_cvt_pk_bf16_f32 v4, v22, v4
	v_pk_mul_f32 v[22:23], v[24:25], v[36:37]
	s_nop 0
	v_sub_f32_e32 v5, v22, v23
	v_pk_mul_f32 v[22:23], v[24:25], v[28:29]
	v_add_u32_e32 v24, 0xb0, v42
	v_add_f32_e32 v22, v23, v22
	v_cvt_pk_bf16_f32 v5, v5, v22
	flat_store_dwordx4 v[50:51], v[2:5] offset:256
	v_mov_b32_e32 v22, 1.0
	v_mov_b32_e32 v23, 0
	v_mov_b32_e32 v2, 1.0
	v_mov_b32_e32 v4, 1.0
	v_mov_b32_e32 v3, 0
	v_mov_b32_e32 v5, 0
	s_cbranch_vccnz .LBB0_204
	v_lshlrev_b32_e32 v0, 8, v24
	v_and_b32_e32 v192, 0x7ff00, v0
	v_lshl_add_u64 v[0:1], s[14:15], 0, v[192:193]
	v_lshl_add_u64 v[4:5], s[16:17], 0, v[192:193]
	v_lshl_add_u64 v[0:1], v[0:1], 0, v[32:33]
	v_lshl_add_u64 v[4:5], v[4:5], 0, v[32:33]
	s_nop 0
	flat_load_dwordx4 v[26:29], v[4:5]
	s_waitcnt vmcnt(0) lgkmcnt(0)
	v_mov_b32_e32 v0, v224
	v_mov_b32_e32 v1, v225
	v_mov_b32_e32 v2, v226
	v_mov_b32_e32 v3, v227
	v_mov_b32_e32 v22, v1
	v_mov_b32_e32 v4, v3
	v_mov_b32_e32 v1, v26
	v_mov_b32_e32 v23, v27
	v_mov_b32_e32 v3, v28
	v_mov_b32_e32 v5, v29
